# gemm W staging de-serialised; agg1 rowptr/adst loads hoisted before barrier
# baseline (speedup 1.0000x reference)
.LBB1_69:
	s_and_b64 vcc, exec, s[4:5]
	s_cbranch_vccz .LBB1_79
	v_lshrrev_b32_e32 v2, 2, v0
	s_load_dwordx4 s[4:7], s[0:1], 0x0
	v_and_b32_e32 v2, 0x70, v2
	v_and_b32_e32 v1, 15, v0
	v_lshl_or_b32 v35, s2, 7, v2
	v_or_b32_e32 v34, v35, v1
	v_min_u32_e32 v2, 0xc34f, v34
	v_bfe_u32 v40, v0, 4, 2
	v_lshlrev_b32_e32 v36, 9, v2
	v_mov_b32_e32 v37, 0
	s_waitcnt vmcnt(0) lgkmcnt(0)
	v_lshl_add_u64 v[2:3], s[4:5], 0, v[36:37]
	v_lshlrev_b32_e32 v36, 5, v40
	v_lshl_add_u64 v[54:55], v[2:3], 0, v[36:37]
	global_load_dwordx4 v[30:33], v[54:55], off offset:16 nt
	global_load_dwordx4 v[18:21], v[54:55], off nt
	global_load_dwordx4 v[14:17], v[54:55], off offset:144 nt
	global_load_dwordx4 v[10:13], v[54:55], off offset:128 nt
	global_load_dwordx4 v[6:9], v[54:55], off offset:272 nt
	global_load_dwordx4 v[2:5], v[54:55], off offset:256 nt
	v_lshlrev_b32_e32 v36, 4, v0
	v_lshl_add_u64 v[38:39], s[6:7], 0, v[36:37]
	global_load_dwordx4 v[42:45], v36, s[6:7]
	v_add_co_u32_e32 v56, vcc, 0x2000, v38
	v_or_b32_e32 v37, 0x4000, v36
	s_nop 0
	v_addc_co_u32_e32 v57, vcc, 0, v39, vcc
	global_load_dwordx4 v[46:49], v[56:57], off
	global_load_dwordx4 v[50:53], v37, s[6:7]
	global_load_dwordx4 v[26:29], v[54:55], off offset:400 nt
	global_load_dwordx4 v[22:25], v[54:55], off offset:384 nt
	v_add_co_u32_e32 v38, vcc, 0x6000, v38
	v_or_b32_e32 v37, 0x800, v0
	v_min_u32_e32 v37, 0x98f, v37
	v_addc_co_u32_e32 v39, vcc, 0, v39, vcc
	global_load_dwordx4 v[58:61], v[38:39], off
	v_lshlrev_b32_e32 v37, 4, v37
	s_waitcnt vmcnt(5)
	ds_write_b128 v36, v[42:45]
	global_load_dwordx4 v[42:45], v37, s[6:7]
	s_movk_i32 s2, 0x190
	v_cmp_gt_u32_e32 vcc, s2, v0
	s_waitcnt vmcnt(5)
	ds_write_b128 v36, v[46:49] offset:8192
	s_waitcnt vmcnt(4)
	ds_write_b128 v36, v[50:53] offset:16384
	s_waitcnt vmcnt(1)
	ds_write_b128 v36, v[58:61] offset:24576
	s_and_saveexec_b64 s[2:3], vcc
	s_waitcnt vmcnt(0)
	ds_write_b128 v36, v[42:45] offset:32768
	s_or_b64 exec, exec, s[2:3]
	s_mov_b32 s2, 0xc350
	v_cmp_gt_u32_e32 vcc, s2, v35
	s_waitcnt lgkmcnt(0)
	s_barrier
	s_and_saveexec_b64 s[2:3], vcc
	s_cbranch_execz .LBB1_79
	v_lshlrev_b32_e32 v36, 3, v40
	v_mul_u32_u24_e32 v1, 0x110, v1
	v_lshl_add_u32 v37, v36, 1, v1
	ds_read_b128 v[42:45], v37
	v_cvt_pk_f16_f32 v33, v32, v33
	v_cvt_pk_f16_f32 v32, v30, v31
	v_cvt_pk_f16_f32 v31, v20, v21
	v_cvt_pk_f16_f32 v30, v18, v19
	ds_read_b128 v[18:21], v37 offset:64
	v_cvt_pk_f16_f32 v17, v16, v17
	v_cvt_pk_f16_f32 v16, v14, v15
	v_cvt_pk_f16_f32 v15, v12, v13
	v_cvt_pk_f16_f32 v14, v10, v11
	ds_read_b128 v[10:13], v37 offset:128
	ds_read_b128 v[46:49], v37 offset:192
	s_waitcnt lgkmcnt(3)
	v_mfma_f32_16x16x32_f16 v[42:45], v[42:45], v[30:33], 0
	v_cvt_pk_f16_f32 v9, v8, v9
	v_cvt_pk_f16_f32 v8, v6, v7
	v_cvt_pk_f16_f32 v7, v4, v5
	s_waitcnt lgkmcnt(2)
	v_mfma_f32_16x16x32_f16 v[18:21], v[18:21], v[14:17], v[42:45]
	v_cvt_pk_f16_f32 v6, v2, v3
	s_waitcnt vmcnt(0)
	v_cvt_pk_f16_f32 v3, v24, v25
	v_cvt_pk_f16_f32 v2, v22, v23
	s_waitcnt lgkmcnt(1)
	v_mfma_f32_16x16x32_f16 v[10:13], v[10:13], v[6:9], v[18:21]
	ds_read_b128 v[22:25], v37 offset:4416
	v_cvt_pk_f16_f32 v5, v28, v29
	v_cvt_pk_f16_f32 v4, v26, v27
	ds_read_b128 v[18:21], v37 offset:4352
	s_waitcnt lgkmcnt(0)
	v_mfma_f32_16x16x32_f16 v[18:21], v[18:21], v[30:33], 0
	ds_read_b128 v[26:29], v37 offset:4480
	ds_read_b128 v[42:45], v37 offset:8832
	ds_read_b128 v[50:53], v37 offset:17536
	v_mfma_f32_16x16x32_f16 v[18:21], v[22:25], v[14:17], v[18:21]
	ds_read_b128 v[22:25], v37 offset:4544
	ds_read_b128 v[54:57], v37 offset:21888
	v_mov_b32_e32 v35, 0
	s_waitcnt lgkmcnt(4)
	v_mfma_f32_16x16x32_f16 v[18:21], v[26:29], v[6:9], v[18:21]
	ds_read_b128 v[26:29], v37 offset:8704
	v_mov_b32_e32 v62, v35
	v_mov_b32_e32 v63, v35
	s_waitcnt lgkmcnt(2)
	v_mfma_f32_16x16x32_f16 v[18:21], v[22:25], v[2:5], v[18:21]
	ds_read_b128 v[22:25], v37 offset:8768
	s_load_dwordx2 s[2:3], s[0:1], 0x10
	v_lshrrev_b32_e32 v1, 4, v0
	s_waitcnt lgkmcnt(0)
	v_mfma_f32_16x16x32_f16 v[26:29], v[26:29], v[30:33], 0
	v_lshlrev_b64 v[38:39], 7, v[34:35]
	s_nop 1
	v_cvt_pk_fp8_f32 v63, v18, v19
	v_lshlrev_b32_e32 v1, 2, v1
	v_mfma_f32_16x16x32_f16 v[22:25], v[22:25], v[14:17], v[26:29]
	v_lshl_add_u64 v[38:39], s[2:3], 0, v[38:39]
	v_cvt_pk_fp8_f32 v63, v20, v21 op_sel:[0,0,1]
	v_and_b32_e32 v0, 16, v0
	ds_read_b128 v[26:29], v37 offset:8896
	v_mfma_f32_16x16x32_f16 v[22:25], v[42:45], v[6:9], v[22:25]
	ds_read_b128 v[42:45], v37 offset:13056
	v_cmp_lt_u32_e32 vcc, 1, v40
	s_waitcnt lgkmcnt(1)
	v_mfma_f32_16x16x32_f16 v[22:25], v[26:29], v[2:5], v[22:25]
	ds_read_b128 v[26:29], v37 offset:13120
	v_mfma_f32_16x16x32_f16 v[10:13], v[46:49], v[2:5], v[10:13]
	ds_read_b128 v[46:49], v37 offset:13184
	s_waitcnt lgkmcnt(2)
	v_mfma_f32_16x16x32_f16 v[42:45], v[42:45], v[30:33], 0
	s_waitcnt lgkmcnt(1)
	v_mfma_f32_16x16x32_f16 v[26:29], v[26:29], v[14:17], v[42:45]
	s_nop 2
	v_cvt_pk_fp8_f32 v62, v10, v11
	v_cvt_pk_fp8_f32 v62, v12, v13 op_sel:[0,0,1]
	s_nop 0
	ds_read_b128 v[42:45], v37 offset:13248
	s_waitcnt lgkmcnt(1)
	v_mfma_f32_16x16x32_f16 v[26:29], v[46:49], v[6:9], v[26:29]
	ds_read_b128 v[46:49], v37 offset:17408
	v_permlane16_swap_b32_e32 v62, v63
	s_waitcnt lgkmcnt(1)
	v_mfma_f32_16x16x32_f16 v[26:29], v[42:45], v[2:5], v[26:29]
	ds_read_b128 v[42:45], v37 offset:17472
	s_waitcnt lgkmcnt(1)
	v_mfma_f32_16x16x32_f16 v[46:49], v[46:49], v[30:33], 0
	s_waitcnt lgkmcnt(0)
	v_mfma_f32_16x16x32_f16 v[42:45], v[42:45], v[14:17], v[46:49]
	s_nop 5
	ds_read_b128 v[46:49], v37 offset:17600
	v_mfma_f32_16x16x32_f16 v[42:45], v[50:53], v[6:9], v[42:45]
	ds_read_b128 v[50:53], v37 offset:21760
	s_waitcnt lgkmcnt(1)
	v_mfma_f32_16x16x32_f16 v[42:45], v[46:49], v[2:5], v[42:45]
	ds_read_b128 v[46:49], v37 offset:21824
	s_waitcnt lgkmcnt(1)
	v_mfma_f32_16x16x32_f16 v[50:53], v[50:53], v[30:33], 0
	s_waitcnt lgkmcnt(0)
	v_mfma_f32_16x16x32_f16 v[46:49], v[46:49], v[14:17], v[50:53]
	s_nop 5
	ds_read_b128 v[50:53], v37 offset:21952
	v_mfma_f32_16x16x32_f16 v[46:49], v[54:57], v[6:9], v[46:49]
	ds_read_b128 v[54:57], v37 offset:26112
	ds_read_b128 v[58:61], v37 offset:26176
	ds_read_b128 v[10:13], v37 offset:26240
	s_waitcnt lgkmcnt(2)
	v_mfma_f32_16x16x32_f16 v[18:21], v[54:57], v[30:33], 0
	s_waitcnt lgkmcnt(1)
	v_mfma_f32_16x16x32_f16 v[18:21], v[58:61], v[14:17], v[18:21]
	v_mov_b32_e32 v58, v35
	v_cvt_pk_fp8_f32 v58, v42, v43
	v_mov_b32_e32 v59, v35
	v_mfma_f32_16x16x32_f16 v[46:49], v[50:53], v[2:5], v[46:49]
	v_and_b32_e32 v50, 8, v1
	v_mov_b32_e32 v51, v35
	v_lshl_add_u64 v[38:39], v[38:39], 0, v[50:51]
	ds_read_b128 v[50:53], v37 offset:26304
	s_waitcnt lgkmcnt(1)
	v_mfma_f32_16x16x32_f16 v[10:13], v[10:13], v[6:9], v[18:21]
	s_nop 2
	ds_read_b128 v[18:21], v37 offset:30464
	ds_read_b128 v[54:57], v37 offset:30528
	v_mov_b32_e32 v1, v35
	v_lshl_add_u64 v[0:1], v[38:39], 0, v[0:1]
	v_mov_b32_e32 v38, v35
	v_cvt_pk_fp8_f32 v38, v22, v23
	s_waitcnt lgkmcnt(1)
	v_mfma_f32_16x16x32_f16 v[18:21], v[18:21], v[30:33], 0
	v_mov_b32_e32 v39, v35
	v_cvt_pk_fp8_f32 v39, v26, v27
	v_cvt_pk_fp8_f32 v38, v24, v25 op_sel:[0,0,1]
	v_mfma_f32_16x16x32_f16 v[10:13], v[50:53], v[2:5], v[10:13]
	ds_read_b128 v[22:25], v37 offset:30592
	ds_read_b128 v[50:53], v37 offset:30656
	global_store_dwordx2 v[0:1], v[62:63], off
	v_cvt_pk_fp8_f32 v39, v28, v29 op_sel:[0,0,1]
	s_waitcnt lgkmcnt(2)
	v_mfma_f32_16x16x32_f16 v[18:21], v[54:57], v[14:17], v[18:21]
	ds_read_b128 v[26:29], v37 offset:34816
	ds_read_b128 v[54:57], v37 offset:34880
	v_cvt_pk_fp8_f32 v58, v44, v45 op_sel:[0,0,1]
	v_permlane16_swap_b32_e32 v38, v39
	s_waitcnt lgkmcnt(3)
	v_mfma_f32_16x16x32_f16 v[18:21], v[22:25], v[6:9], v[18:21]
	ds_read_b128 v[22:25], v37 offset:34944
	ds_read_b128 v[42:45], v37 offset:35008
	global_store_dwordx2 v[0:1], v[38:39], off offset:32
	v_mov_b32_e32 v38, v35
	s_waitcnt lgkmcnt(4)
	v_mfma_f32_16x16x32_f16 v[18:21], v[50:53], v[2:5], v[18:21]
	v_mov_b32_e32 v39, v35
	v_cvt_pk_fp8_f32 v59, v46, v47
	v_cvt_pk_fp8_f32 v38, v10, v11
	s_waitcnt lgkmcnt(3)
	v_mfma_f32_16x16x32_f16 v[26:29], v[26:29], v[30:33], 0
	v_cvt_pk_fp8_f32 v59, v48, v49 op_sel:[0,0,1]
	s_nop 1
	v_cvt_pk_fp8_f32 v39, v18, v19
	s_waitcnt lgkmcnt(2)
	v_mfma_f32_16x16x32_f16 v[14:17], v[54:57], v[14:17], v[26:29]
	v_cvt_pk_fp8_f32 v38, v12, v13 op_sel:[0,0,1]
	v_permlane16_swap_b32_e32 v58, v59
	v_cvt_pk_fp8_f32 v39, v20, v21 op_sel:[0,0,1]
	s_waitcnt lgkmcnt(1)
	v_mfma_f32_16x16x32_f16 v[6:9], v[22:25], v[6:9], v[14:17]
	global_store_dwordx2 v[0:1], v[58:59], off offset:64
	v_permlane16_swap_b32_e32 v38, v39
	global_store_dwordx2 v[0:1], v[38:39], off offset:96
	s_waitcnt lgkmcnt(0)
	v_mfma_f32_16x16x32_f16 v[0:3], v[42:45], v[2:5], v[6:9]
	s_and_saveexec_b64 s[2:3], vcc
	s_xor_b64 s[2:3], exec, s[2:3]
	s_cbranch_execz .LBB1_77
	s_load_dwordx2 s[4:5], s[0:1], 0x20
	v_lshlrev_b64 v[4:5], 5, v[34:35]
	v_lshlrev_b32_e32 v34, 4, v40
	s_waitcnt lgkmcnt(0)
	v_lshl_add_u64 v[4:5], s[4:5], 0, v[4:5]
	v_lshl_add_u64 v[4:5], v[4:5], 0, v[34:35]
	global_store_dwordx4 v[4:5], v[0:3], off offset:-32

_Z11agg1_kernelPKDF16_PKfS2_PKiS4_S2_S2_PDF16_PfS6_i:
	s_load_dwordx8 s[4:11], s[0:1], 0x0
	s_load_dwordx8 s[12:19], s[0:1], 0x20
	s_load_dwordx4 s[20:23], s[0:1], 0x40
	s_load_dword s24, s[0:1], 0x50
	v_lshlrev_b32_e32 v22, 2, v0
	v_readfirstlane_b32 s25, v0
	s_lshl_b32 s26, s2, 5
	v_and_b32_e32 v53, 15, v0
	v_bfe_u32 v4, v0, 4, 2
	v_and_b32_e32 v1, 14, v0
	s_lshr_b32 s25, s25, 6
	s_lshl_b32 s27, s25, 3
	s_add_i32 s26, s26, s27
	v_lshlrev_b32_e32 v54, 1, v1
	v_add_u32_e32 v56, s26, v4
	v_add_u32_e32 v57, 4, v56
	s_waitcnt lgkmcnt(0)
	global_load_dword v23, v22, s[14:15]
	global_load_dword v24, v22, s[16:17]
	s_add_i32 s28, s24, -1
	v_cmp_gt_i32_e64 s[36:37], s24, v56
	v_cmp_gt_i32_e64 s[38:39], s24, v57
	v_min_i32_e32 v56, s28, v56
	v_min_i32_e32 v57, s28, v57
	v_lshlrev_b32_e32 v25, 2, v56
	v_lshlrev_b32_e32 v26, 2, v57
	global_load_dword v48, v25, s[10:11]
	global_load_dword v27, v25, s[10:11] offset:4
	global_load_dword v50, v26, s[10:11]
	global_load_dword v28, v26, s[10:11] offset:4
	v_lshl_or_b32 v29, v56, 5, v54
	v_lshl_or_b32 v30, v57, 5, v54
	global_load_dword v7, v29, s[8:9]
	global_load_dword v10, v30, s[8:9]
	s_cmp_le_i32 s24, s26
	s_waitcnt vmcnt(6)
	ds_write2st64_b32 v22, v23, v24 offset0:32 offset1:36
	s_waitcnt lgkmcnt(0)
	s_barrier
	s_cbranch_scc1 .Lagg_exit
	v_and_b32_e32 v2, 1, v0
	v_lshlrev_b32_e32 v2, 3, v2
	v_lshlrev_b32_e32 v3, 7, v53
	v_lshl_add_u32 v3, v4, 1, v3
	s_lshl_b32 s27, s25, 11
	v_add_u32_e32 v3, s27, v3
	v_lshlrev_b32_e32 v52, 5, v53
	v_add_u32_e32 v52, 0x2000, v52
	v_cmp_eq_u32_e64 s[34:35], 0, v53
	v_and_b32_e32 v5, 63, v0
	v_lshlrev_b32_e32 v5, 5, v5
	v_add_u32_e32 v55, s27, v5
	v_mov_b32_e32 v32, 0
	v_mov_b32_e32 v33, 0
	v_mov_b32_e32 v34, 0
	v_mov_b32_e32 v35, 0
	ds_write_b128 v55, v[32:35]
	ds_write_b128 v55, v[32:35] offset:16
	v_mov_b32_e32 v4, v25
	v_mov_b32_e32 v22, v56
	v_mov_b32_e32 v23, v57
	s_waitcnt vmcnt(2)
	v_sub_u32_e32 v49, v27, v48
	v_sub_u32_e32 v51, v28, v50
	v_add_u32_e32 v49, 1, v49
	v_add_u32_e32 v51, 1, v51
	s_nop 0
	v_readlane_b32 s29, v49, 0
	v_readlane_b32 s27, v49, 16
	v_readlane_b32 s40, v49, 32
	v_readlane_b32 s41, v49, 48
	s_max_i32 s29, s29, s27
	s_max_i32 s40, s40, s41
	s_max_i32 s29, s29, s40
	v_readlane_b32 s30, v51, 0
	v_readlane_b32 s27, v51, 16
	v_readlane_b32 s40, v51, 32
	v_readlane_b32 s41, v51, 48
	s_max_i32 s30, s30, s27
	s_max_i32 s40, s40, s41
	s_max_i32 s30, s30, s40
	v_add_u32_e32 v30, v48, v53
	v_lshlrev_b32_e32 v30, 2, v30
	v_mov_b32_e32 v5, s24
	v_mov_b32_e32 v6, s24
	v_cndmask_b32_e64 v5, v5, v22, s[34:35]
	v_cmp_gt_i32_e32 vcc, v49, v53
	s_andn2_b64 s[40:41], vcc, s[34:35]
	s_and_saveexec_b64 s[32:33], s[40:41]
	global_load_dword v5, v30, s[12:13] offset:-4
	s_mov_b64 exec, s[32:33]
	v_add_u32_e32 v31, 16, v53
	v_cmp_gt_i32_e32 vcc, v49, v31
	s_and_saveexec_b64 s[32:33], vcc
	global_load_dword v6, v30, s[12:13] offset:60
	s_mov_b64 exec, s[32:33]
	v_add_u32_e32 v30, v50, v53
	v_lshlrev_b32_e32 v30, 2, v30
	v_mov_b32_e32 v8, s24
	v_mov_b32_e32 v9, s24
	v_cndmask_b32_e64 v8, v8, v23, s[34:35]
	v_cmp_gt_i32_e32 vcc, v51, v53
	s_andn2_b64 s[40:41], vcc, s[34:35]
	s_and_saveexec_b64 s[32:33], s[40:41]
	global_load_dword v8, v30, s[12:13] offset:-4
	s_mov_b64 exec, s[32:33]
	v_add_u32_e32 v31, 16, v53
	v_cmp_gt_i32_e32 vcc, v51, v31
	s_and_saveexec_b64 s[32:33], vcc
	global_load_dword v9, v30, s[12:13] offset:60
	s_mov_b64 exec, s[32:33]
	s_waitcnt vmcnt(0)
	v_lshlrev_b32_e32 v5, 4, v5
	v_lshlrev_b32_e32 v6, 4, v6
	v_lshlrev_b32_e32 v8, 4, v8
	v_lshlrev_b32_e32 v9, 4, v9
	s_mov_b32 s31, 0

	.amdhsa_kernel _Z11agg1_kernelPKDF16_PKfS2_PKiS4_S2_S2_PDF16_PfS6_i
		.amdhsa_group_segment_fixed_size 10240
		.amdhsa_private_segment_fixed_size 0
		.amdhsa_kernarg_size 84
		.amdhsa_user_sgpr_count 2
		.amdhsa_user_sgpr_dispatch_ptr 0
		.amdhsa_user_sgpr_queue_ptr 0
		.amdhsa_user_sgpr_kernarg_segment_ptr 1
		.amdhsa_user_sgpr_dispatch_id 0
		.amdhsa_user_sgpr_kernarg_preload_length 0
		.amdhsa_user_sgpr_kernarg_preload_offset 0
		.amdhsa_user_sgpr_private_segment_size 0
		.amdhsa_uses_dynamic_stack 0
		.amdhsa_enable_private_segment 0
		.amdhsa_system_sgpr_workgroup_id_x 1
		.amdhsa_system_sgpr_workgroup_id_y 0
		.amdhsa_system_sgpr_workgroup_id_z 0
		.amdhsa_system_sgpr_workgroup_info 0
		.amdhsa_system_vgpr_workitem_id 0
		.amdhsa_next_free_vgpr 58
		.amdhsa_next_free_sgpr 44
		.amdhsa_accum_offset 60
		.amdhsa_reserve_vcc 1
		.amdhsa_float_round_mode_32 0
		.amdhsa_float_round_mode_16_64 0
		.amdhsa_float_denorm_mode_32 3
		.amdhsa_float_denorm_mode_16_64 3
		.amdhsa_dx10_clamp 1
		.amdhsa_ieee_mode 1
		.amdhsa_fp16_overflow 0
		.amdhsa_tg_split 0
		.amdhsa_exception_fp_ieee_invalid_op 0
		.amdhsa_exception_fp_denorm_src 0
		.amdhsa_exception_fp_ieee_div_zero 0
		.amdhsa_exception_fp_ieee_overflow 0
		.amdhsa_exception_fp_ieee_underflow 0
		.amdhsa_exception_fp_ieee_inexact 0
		.amdhsa_exception_int_div_zero 0
	.end_amdhsa_kernel

amdhsa.kernels:
  - .agpr_count:     0
    .args:
      - .actual_access:  read_only
        .address_space:  global
        .offset:         0
        .size:           8
        .value_kind:     global_buffer
      - .actual_access:  read_only
        .address_space:  global
        .offset:         8
        .size:           8
        .value_kind:     global_buffer
      - .actual_access:  read_only
        .address_space:  global
        .offset:         16
        .size:           8
        .value_kind:     global_buffer
      - .actual_access:  read_only
        .address_space:  global
        .offset:         24
        .size:           8
        .value_kind:     global_buffer
      - .actual_access:  read_only
        .address_space:  global
        .offset:         32
        .size:           8
        .value_kind:     global_buffer
      - .actual_access:  read_only
        .address_space:  global
        .offset:         40
        .size:           8
        .value_kind:     global_buffer
      - .actual_access:  read_only
        .address_space:  global
        .offset:         48
        .size:           8
        .value_kind:     global_buffer
      - .actual_access:  read_only
        .address_space:  global
        .offset:         56
        .size:           8
        .value_kind:     global_buffer
      - .actual_access:  read_only
        .address_space:  global
        .offset:         64
        .size:           8
        .value_kind:     global_buffer
      - .actual_access:  read_only
        .address_space:  global
        .offset:         72
        .size:           8
        .value_kind:     global_buffer
      - .actual_access:  read_only
        .address_space:  global
        .offset:         80
        .size:           8
        .value_kind:     global_buffer
      - .actual_access:  read_only
        .address_space:  global
        .offset:         88
        .size:           8
        .value_kind:     global_buffer
      - .actual_access:  read_only
        .address_space:  global
        .offset:         96
        .size:           8
        .value_kind:     global_buffer
      - .actual_access:  write_only
        .address_space:  global
        .offset:         104
        .size:           8
        .value_kind:     global_buffer
      - .actual_access:  write_only
        .address_space:  global
        .offset:         112
        .size:           8
        .value_kind:     global_buffer
      - .actual_access:  write_only
        .address_space:  global
        .offset:         120
        .size:           8
        .value_kind:     global_buffer
      - .actual_access:  write_only
        .address_space:  global
        .offset:         128
        .size:           8
        .value_kind:     global_buffer
      - .actual_access:  write_only
        .address_space:  global
        .offset:         136
        .size:           8
        .value_kind:     global_buffer
      - .actual_access:  write_only
        .address_space:  global
        .offset:         144
        .size:           8
        .value_kind:     global_buffer
      - .actual_access:  write_only
        .address_space:  global
        .offset:         152
        .size:           8
        .value_kind:     global_buffer
      - .actual_access:  write_only
        .address_space:  global
        .offset:         160
        .size:           8
        .value_kind:     global_buffer
      - .actual_access:  write_only
        .address_space:  global
        .offset:         168
        .size:           8
        .value_kind:     global_buffer
      - .actual_access:  read_only
        .address_space:  global
        .offset:         176
        .size:           8
        .value_kind:     global_buffer
    .group_segment_fixed_size: 29696
    .kernarg_segment_align: 8
    .kernarg_segment_size: 184
    .language:       OpenCL C
    .language_version:
      - 2
      - 0
    .max_flat_workgroup_size: 512
    .name:           _Z12front_kernelPKiS0_PKfS2_S2_S2_S2_S2_S2_S2_S2_S2_S2_PjS3_PiS4_PDF16_PfS6_S4_S5_S0_
    .private_segment_fixed_size: 0
    .sgpr_count:     30
    .sgpr_spill_count: 0
    .symbol:         _Z12front_kernelPKiS0_PKfS2_S2_S2_S2_S2_S2_S2_S2_S2_S2_PjS3_PiS4_PDF16_PfS6_S4_S5_S0_.kd
    .uniform_work_group_size: 1
    .uses_dynamic_stack: false
    .vgpr_count:     80
    .vgpr_spill_count: 0
    .wavefront_size: 64
  - .agpr_count:     0
    .args:
      - .actual_access:  read_only
        .address_space:  global
        .offset:         0
        .size:           8
        .value_kind:     global_buffer
      - .actual_access:  read_only
        .address_space:  global
        .offset:         8
        .size:           8
        .value_kind:     global_buffer
      - .actual_access:  write_only
        .address_space:  global
        .offset:         16
        .size:           8
        .value_kind:     global_buffer
      - .actual_access:  write_only
        .address_space:  global
        .offset:         24
        .size:           8
        .value_kind:     global_buffer
      - .actual_access:  write_only
        .address_space:  global
        .offset:         32
        .size:           8
        .value_kind:     global_buffer
      - .actual_access:  read_only
        .address_space:  global
        .offset:         40
        .size:           8
        .value_kind:     global_buffer
      - .actual_access:  read_only
        .address_space:  global
        .offset:         48
        .size:           8
        .value_kind:     global_buffer
      - .actual_access:  write_only
        .address_space:  global
        .offset:         56
        .size:           8
        .value_kind:     global_buffer
      - .actual_access:  write_only
        .address_space:  global
        .offset:         64
        .size:           8
        .value_kind:     global_buffer
    .group_segment_fixed_size: 40960
    .kernarg_segment_align: 8
    .kernarg_segment_size: 72
    .language:       OpenCL C
    .language_version:
      - 2
      - 0
    .max_flat_workgroup_size: 512
    .name:           _Z13second_kernelPKfPKDF16_PDF16_PfS4_PKjPKiPiS9_
    .private_segment_fixed_size: 0
    .sgpr_count:     29
    .sgpr_spill_count: 0
    .symbol:         _Z13second_kernelPKfPKDF16_PDF16_PfS4_PKjPKiPiS9_.kd
    .uniform_work_group_size: 1
    .uses_dynamic_stack: false
    .vgpr_count:     64
    .vgpr_spill_count: 0
    .wavefront_size: 64
  - .agpr_count:     0
    .args:
      - .actual_access:  read_only
        .address_space:  global
        .offset:         0
        .size:           8
        .value_kind:     global_buffer
      - .actual_access:  read_only
        .address_space:  global
        .offset:         8
        .size:           8
        .value_kind:     global_buffer
      - .actual_access:  read_only
        .address_space:  global
        .offset:         16
        .size:           8
        .value_kind:     global_buffer
      - .actual_access:  read_only
        .address_space:  global
        .offset:         24
        .size:           8
        .value_kind:     global_buffer
      - .actual_access:  read_only
        .address_space:  global
        .offset:         32
        .size:           8
        .value_kind:     global_buffer
      - .actual_access:  read_only
        .address_space:  global
        .offset:         40
        .size:           8
        .value_kind:     global_buffer
      - .actual_access:  read_only
        .address_space:  global
        .offset:         48
        .size:           8
        .value_kind:     global_buffer
      - .actual_access:  write_only
        .address_space:  global
        .offset:         56
        .size:           8
        .value_kind:     global_buffer
      - .actual_access:  write_only
        .address_space:  global
        .offset:         64
        .size:           8
        .value_kind:     global_buffer
      - .actual_access:  write_only
        .address_space:  global
        .offset:         72
        .size:           8
        .value_kind:     global_buffer
      - .offset:         80
        .size:           4
        .value_kind:     by_value
    .group_segment_fixed_size: 10240
    .kernarg_segment_align: 8
    .kernarg_segment_size: 84
    .language:       OpenCL C
    .language_version:
      - 2
      - 0
    .max_flat_workgroup_size: 256
    .name:           _Z11agg1_kernelPKDF16_PKfS2_PKiS4_S2_S2_PDF16_PfS6_i
    .private_segment_fixed_size: 0
    .sgpr_count:     50
    .sgpr_spill_count: 0
    .symbol:         _Z11agg1_kernelPKDF16_PKfS2_PKiS4_S2_S2_PDF16_PfS6_i.kd
    .uniform_work_group_size: 1
    .uses_dynamic_stack: false
    .vgpr_count:     58
    .vgpr_spill_count: 0
    .wavefront_size: 64
  - .agpr_count:     0
    .args:
      - .actual_access:  read_only
        .address_space:  global
        .offset:         0
        .size:           8
        .value_kind:     global_buffer
      - .actual_access:  read_only
        .address_space:  global
        .offset:         8
        .size:           8
        .value_kind:     global_buffer
      - .actual_access:  read_only
        .address_space:  global
        .offset:         16
        .size:           8
        .value_kind:     global_buffer
      - .actual_access:  read_only
        .address_space:  global
        .offset:         24
        .size:           8
        .value_kind:     global_buffer
      - .actual_access:  read_only
        .address_space:  global
        .offset:         32
        .size:           8
        .value_kind:     global_buffer
      - .actual_access:  write_only
        .address_space:  global
        .offset:         40
        .size:           8
        .value_kind:     global_buffer
      - .offset:         48
        .size:           4
        .value_kind:     by_value
    .group_segment_fixed_size: 0
    .kernarg_segment_align: 8
    .kernarg_segment_size: 52
    .language:       OpenCL C
    .language_version:
      - 2
      - 0
    .max_flat_workgroup_size: 256
    .name:           _Z13stats2_kernelPKiS0_PKfS2_S0_P15HIP_vector_typeIfLj4EEi
    .private_segment_fixed_size: 0
    .sgpr_count:     27
    .sgpr_spill_count: 0
    .symbol:         _Z13stats2_kernelPKiS0_PKfS2_S0_P15HIP_vector_typeIfLj4EEi.kd
    .uniform_work_group_size: 1
    .uses_dynamic_stack: false
    .vgpr_count:     32
    .vgpr_spill_count: 0
    .wavefront_size: 64
  - .agpr_count:     0
    .args:
      - .actual_access:  read_only
        .address_space:  global
        .offset:         0
        .size:           8
        .value_kind:     global_buffer
      - .actual_access:  read_only
        .address_space:  global
        .offset:         8
        .size:           8
        .value_kind:     global_buffer
      - .actual_access:  read_only
        .address_space:  global
        .offset:         16
        .size:           8
        .value_kind:     global_buffer
      - .actual_access:  read_only
        .address_space:  global
        .offset:         24
        .size:           8
        .value_kind:     global_buffer
      - .actual_access:  read_only
        .address_space:  global
        .offset:         32
        .size:           8
        .value_kind:     global_buffer
      - .actual_access:  write_only
        .address_space:  global
        .offset:         40
        .size:           8
        .value_kind:     global_buffer
      - .offset:         48
        .size:           4
        .value_kind:     by_value
    .group_segment_fixed_size: 69728
    .kernarg_segment_align: 8
    .kernarg_segment_size: 52
    .language:       OpenCL C
    .language_version:
      - 2
      - 0
    .max_flat_workgroup_size: 1024
    .name:           _Z12pool2_kernelPKjPKiPKfPK15HIP_vector_typeIfLj4EEPKDF16_Pfi
    .private_segment_fixed_size: 0
    .sgpr_count:     26
    .sgpr_spill_count: 0
    .symbol:         _Z12pool2_kernelPKjPKiPKfPK15HIP_vector_typeIfLj4EEPKDF16_Pfi.kd
    .uniform_work_group_size: 1
    .uses_dynamic_stack: false
    .vgpr_count:     123
    .vgpr_spill_count: 0
    .wavefront_size: 64
  - .agpr_count:     0
    .args:
      - .actual_access:  read_only
        .address_space:  global
        .offset:         0
        .size:           8
        .value_kind:     global_buffer
      - .actual_access:  read_only
        .address_space:  global
        .offset:         8
        .size:           8
        .value_kind:     global_buffer
      - .actual_access:  read_only
        .address_space:  global
        .offset:         16
        .size:           8
        .value_kind:     global_buffer
      - .actual_access:  read_only
        .address_space:  global
        .offset:         24
        .size:           8
        .value_kind:     global_buffer
      - .actual_access:  read_only
        .address_space:  global
        .offset:         32
        .size:           8
        .value_kind:     global_buffer
      - .actual_access:  read_only
        .address_space:  global
        .offset:         40
        .size:           8
        .value_kind:     global_buffer
      - .actual_access:  read_only
        .address_space:  global
        .offset:         48
        .size:           8
        .value_kind:     global_buffer
      - .actual_access:  read_only
        .address_space:  global
        .offset:         56
        .size:           8
        .value_kind:     global_buffer
      - .actual_access:  write_only
        .address_space:  global
        .offset:         64
        .size:           8
        .value_kind:     global_buffer
    .group_segment_fixed_size: 9472
    .kernarg_segment_align: 8
    .kernarg_segment_size: 72
    .language:       OpenCL C
    .language_version:
      - 2
      - 0
    .max_flat_workgroup_size: 1024
    .name:           _Z10mlp_kernelPKfPKiS0_S0_S0_S0_S0_S0_Pf
    .private_segment_fixed_size: 0
    .sgpr_count:     38
    .sgpr_spill_count: 0
    .symbol:         _Z10mlp_kernelPKfPKiS0_S0_S0_S0_S0_S0_Pf.kd
    .uniform_work_group_size: 1
    .uses_dynamic_stack: false
    .vgpr_count:     64
    .vgpr_spill_count: 0
    .wavefront_size: 64
